# baseline (speedup 1.0000x reference)
_Z6gemm_gILi64ELi64ELi32ELi32ELi1ELi0ELi64ELi4EEv5GemmP:
	s_lshl_b32 s90, s3, 7
	s_add_u32 s90, s90, s2
	s_and_b32 s91, s90, 7
	s_lshr_b32 s90, s90, 3
	s_and_b32 s3, s90, 1
	s_lshr_b32 s92, s90, 5
	s_lshl_b32 s92, s92, 1
	s_or_b32 s3, s3, s92
	s_bfe_u32 s90, s90, 0x40001
	s_lshl_b32 s91, s91, 4
	s_or_b32 s2, s91, s90
	s_load_dwordx4 s[8:11], s[0:1], 0x0
	s_load_dwordx4 s[4:7], s[0:1], 0x38
	s_load_dwordx2 s[12:13], s[0:1], 0x68
	v_lshrrev_b32_e32 v1, 3, v0
	v_xor_b32_e32 v2, v1, v0
	s_waitcnt lgkmcnt(0)
	s_lshl_b32 s7, s2, 6
	v_lshlrev_b32_e32 v2, 3, v2
	v_and_b32_e32 v2, 56, v2
	v_or_b32_e32 v3, s7, v1
	v_mad_u64_u32 v[4:5], s[14:15], v3, s5, v[2:3]
	v_or_b32_e32 v5, 0x100, v0
	v_lshrrev_b32_e32 v5, 3, v5
	v_xor_b32_e32 v6, v5, v0
	v_lshlrev_b32_e32 v6, 3, v6
	v_and_b32_e32 v6, 56, v6
	v_or_b32_e32 v7, s7, v5
	s_and_b32 s16, s2, 63
	v_mad_u64_u32 v[8:9], s[14:15], v7, s5, v[6:7]
	s_lshl_b32 s2, s3, 6
	v_readfirstlane_b32 s22, v0
	v_or_b32_e32 v9, s2, v1
	s_lshr_b32 s21, s22, 6
	v_mad_i64_i32 v[10:11], s[14:15], v9, s4, 0
	v_or_b32_e32 v9, s2, v5
	v_lshl_add_u64 v[10:11], v[10:11], 1, s[10:11]
	v_lshlrev_b32_e32 v12, 1, v2
	v_mov_b32_e32 v13, 0
	v_mad_i64_i32 v[16:17], s[14:15], v9, s4, 0
	s_lshl_b32 s3, s21, 10
	v_lshl_add_u64 v[10:11], v[10:11], 0, v[12:13]
	v_lshl_add_u64 v[16:17], v[16:17], 1, s[10:11]
	v_lshlrev_b32_e32 v12, 1, v6
	s_cmp_lt_i32 s4, 64
	v_mov_b32_e32 v15, s16
	v_lshl_add_u64 v[12:13], v[16:17], 0, v[12:13]
	s_cselect_b64 s[18:19], -1, 0
	s_cmp_gt_i32 s4, 63
	s_mov_b32 s7, 0
	v_cmp_ne_u32_e64 s[14:15], s16, 0
	s_mov_b32 s20, 0
	s_mov_b32 s10, 0
	s_cbranch_scc1 .LBB7_3
	s_cmpk_lt_i32 s4, 0x80
	s_cbranch_scc0 .LBB7_4
